# grid barrier: leader invalidates behind its top-level arrival atomic (off the write-back path), non-leaders at the head of their wait
# baseline (speedup 1.0000x reference)
.LBB0_139:
	v_readlane_b32 s6, v255, 4
	v_readlane_b32 s7, v255, 5
	s_lshl_b64 s[6:7], s[6:7], 2
	v_readlane_b32 s3, v255, 2
	s_add_u32 s8, s3, s6
	v_readlane_b32 s3, v255, 3
	s_addc_u32 s9, s3, s7
	v_readlane_b32 s3, v255, 6
	s_lshl_b32 s3, s3, 8
	s_add_u32 s6, s8, s3
	s_addc_u32 s7, s9, 0
	v_mov_b32_e32 v2, 0x1000
	v_mov_b32_e32 v4, 1
	global_atomic_add v4, v2, v4, s[6:7] offset:1024 sc0
	v_cvt_f32_u32_e32 v2, v3
	v_sub_u32_e32 v5, 0, v3
	v_rcp_iflag_f32_e32 v2, v2
	s_nop 0
	v_mul_f32_e32 v2, 0x4f7ffffe, v2
	v_cvt_u32_f32_e32 v2, v2
	v_mul_lo_u32 v5, v5, v2
	v_mul_hi_u32 v5, v2, v5
	v_add_u32_e32 v2, v2, v5
	s_waitcnt vmcnt(0)
	v_mul_hi_u32 v2, v4, v2
	v_mul_lo_u32 v5, v2, v3
	v_sub_u32_e32 v5, v4, v5
	v_add_u32_e32 v6, 1, v2
	v_cmp_ge_u32_e32 vcc, v5, v3
	v_add_u32_e32 v4, 1, v4
	s_nop 0
	v_cndmask_b32_e32 v2, v2, v6, vcc
	v_sub_u32_e32 v6, v5, v3
	v_cndmask_b32_e32 v5, v5, v6, vcc
	v_add_u32_e32 v6, 1, v2
	v_cmp_ge_u32_e32 vcc, v5, v3
	s_nop 1
	v_cndmask_b32_e32 v2, v2, v6, vcc
	v_mul_lo_u32 v5, v3, v2
	v_add_u32_e32 v3, v5, v3
	v_cmp_ne_u32_e32 vcc, v4, v3
	s_and_saveexec_b64 s[12:13], vcc
	s_xor_b64 s[12:13], exec, s[12:13]
	s_cbranch_execz .LBB0_153
	s_waitcnt lgkmcnt(0)
	v_mov_b32_e32 v1, 0x2000
	buffer_inv sc1
	global_load_dword v1, v1, s[6:7] offset:1024 sc1
	s_add_u32 s16, s6, 0x2400
	s_addc_u32 s17, s7, 0
	s_waitcnt vmcnt(0)
	v_cmp_eq_u32_e32 vcc, v1, v2
	s_and_saveexec_b64 s[14:15], vcc
	s_cbranch_execz .LBB0_152
	s_mov_b32 s3, 1
	s_mov_b64 s[18:19], 0
	v_mov_b32_e32 v1, 0
	s_branch .LBB0_143

.LBB0_153:
	s_andn2_saveexec_b64 s[12:13], s[12:13]
	s_cbranch_execz .LBB0_171
	s_mov_b64 s[12:13], exec
	buffer_wbl2 sc1
	s_waitcnt lgkmcnt(0)
	s_waitcnt vmcnt(0)
	v_mbcnt_lo_u32_b32 v2, s12, 0
	v_mbcnt_hi_u32_b32 v2, s13, v2
	v_cmp_eq_u32_e32 vcc, 0, v2
	s_and_saveexec_b64 s[14:15], vcc
	s_cbranch_execz .LBB0_156
	s_bcnt1_i32_b64 s3, s[12:13]
	v_mov_b32_e32 v3, 0x3000
	v_mov_b32_e32 v4, s3
	global_atomic_add v3, v3, v4, s[8:9] offset:1024 sc0
	buffer_inv sc1
.LBB0_156:
	s_or_b64 exec, exec, s[14:15]
	v_cvt_f32_u32_e32 v4, v1
	s_waitcnt vmcnt(1)
	v_readfirstlane_b32 s3, v3
	s_add_u32 s14, s8, 0x3500
	s_addc_u32 s15, s9, 0
	v_rcp_iflag_f32_e32 v4, v4
	v_add_u32_e32 v2, s3, v2
	v_add_u32_e32 v5, 1, v2
	s_mov_b64 s[16:17], -1
	v_mul_f32_e32 v3, 0x4f7ffffe, v4
	v_cvt_u32_f32_e32 v3, v3
	v_sub_u32_e32 v4, 0, v1
	v_mul_lo_u32 v4, v4, v3
	v_mul_hi_u32 v4, v3, v4
	v_add_u32_e32 v3, v3, v4
	v_mul_hi_u32 v3, v2, v3
	v_mul_lo_u32 v4, v3, v1
	v_sub_u32_e32 v2, v2, v4
	v_add_u32_e32 v6, 1, v3
	v_cmp_ge_u32_e32 vcc, v2, v1
	v_sub_u32_e32 v4, v2, v1
	s_nop 0
	v_cndmask_b32_e32 v3, v3, v6, vcc
	v_cndmask_b32_e32 v2, v2, v4, vcc
	v_add_u32_e32 v4, 1, v3
	v_cmp_ge_u32_e32 vcc, v2, v1
	s_nop 1
	v_cndmask_b32_e32 v4, v3, v4, vcc
	v_mul_lo_u32 v2, v1, v4
	v_add_u32_e32 v1, v2, v1
	v_cmp_ne_u32_e32 vcc, v5, v1
	v_mov_b64_e32 v[2:3], s[14:15]
	s_and_saveexec_b64 s[12:13], vcc
	s_cbranch_execz .LBB0_168
	v_mov_b32_e32 v1, 0
	global_load_dword v2, v1, s[14:15] sc1
	s_mov_b64 s[20:21], 0
	s_waitcnt vmcnt(0)
	v_cmp_eq_u32_e32 vcc, v2, v4
	s_and_saveexec_b64 s[18:19], vcc
	s_cbranch_execz .LBB0_167
	s_add_u32 s16, s8, 0x200
	s_addc_u32 s17, s9, 0
	s_mov_b32 s3, 1
	s_mov_b64 s[8:9], 0
	s_branch .LBB0_160

.LBB0_193:
	v_readlane_b32 s6, v255, 4
	v_readlane_b32 s7, v255, 5
	s_lshl_b64 s[6:7], s[6:7], 2
	v_readlane_b32 s3, v255, 2
	s_add_u32 s8, s3, s6
	v_readlane_b32 s3, v255, 3
	s_addc_u32 s9, s3, s7
	v_readlane_b32 s3, v255, 6
	s_lshl_b32 s3, s3, 8
	s_add_u32 s6, s8, s3
	s_addc_u32 s7, s9, 0
	v_mov_b32_e32 v2, 0x1000
	v_mov_b32_e32 v4, 1
	global_atomic_add v4, v2, v4, s[6:7] offset:1024 sc0
	v_cvt_f32_u32_e32 v2, v3
	v_sub_u32_e32 v5, 0, v3
	v_rcp_iflag_f32_e32 v2, v2
	s_nop 0
	v_mul_f32_e32 v2, 0x4f7ffffe, v2
	v_cvt_u32_f32_e32 v2, v2
	v_mul_lo_u32 v5, v5, v2
	v_mul_hi_u32 v5, v2, v5
	v_add_u32_e32 v2, v2, v5
	s_waitcnt vmcnt(0)
	v_mul_hi_u32 v2, v4, v2
	v_mul_lo_u32 v5, v2, v3
	v_sub_u32_e32 v5, v4, v5
	v_add_u32_e32 v6, 1, v2
	v_cmp_ge_u32_e32 vcc, v5, v3
	v_add_u32_e32 v4, 1, v4
	s_nop 0
	v_cndmask_b32_e32 v2, v2, v6, vcc
	v_sub_u32_e32 v6, v5, v3
	v_cndmask_b32_e32 v5, v5, v6, vcc
	v_add_u32_e32 v6, 1, v2
	v_cmp_ge_u32_e32 vcc, v5, v3
	s_nop 1
	v_cndmask_b32_e32 v2, v2, v6, vcc
	v_mul_lo_u32 v5, v3, v2
	v_add_u32_e32 v3, v5, v3
	v_cmp_ne_u32_e32 vcc, v4, v3
	s_and_saveexec_b64 s[10:11], vcc
	s_xor_b64 s[10:11], exec, s[10:11]
	s_cbranch_execz .LBB0_207
	s_waitcnt lgkmcnt(0)
	v_mov_b32_e32 v1, 0x2000
	buffer_inv sc1
	global_load_dword v1, v1, s[6:7] offset:1024 sc1
	s_add_u32 s14, s6, 0x2400
	s_addc_u32 s15, s7, 0
	s_waitcnt vmcnt(0)
	v_cmp_eq_u32_e32 vcc, v1, v2
	s_and_saveexec_b64 s[12:13], vcc
	s_cbranch_execz .LBB0_206
	s_mov_b32 s3, 1
	s_mov_b64 s[16:17], 0
	v_mov_b32_e32 v1, 0
	s_branch .LBB0_197

.LBB0_207:
	s_andn2_saveexec_b64 s[10:11], s[10:11]
	s_cbranch_execz .LBB0_225
	s_mov_b64 s[10:11], exec
	buffer_wbl2 sc1
	s_waitcnt lgkmcnt(0)
	s_waitcnt vmcnt(0)
	v_mbcnt_lo_u32_b32 v2, s10, 0
	v_mbcnt_hi_u32_b32 v2, s11, v2
	v_cmp_eq_u32_e32 vcc, 0, v2
	s_and_saveexec_b64 s[12:13], vcc
	s_cbranch_execz .LBB0_210
	s_bcnt1_i32_b64 s3, s[10:11]
	v_mov_b32_e32 v3, 0x3000
	v_mov_b32_e32 v4, s3
	global_atomic_add v3, v3, v4, s[8:9] offset:1024 sc0
	buffer_inv sc1
.LBB0_210:
	s_or_b64 exec, exec, s[12:13]
	v_cvt_f32_u32_e32 v4, v1
	s_waitcnt vmcnt(1)
	v_readfirstlane_b32 s3, v3
	s_add_u32 s12, s8, 0x3500
	s_addc_u32 s13, s9, 0
	v_rcp_iflag_f32_e32 v4, v4
	v_add_u32_e32 v2, s3, v2
	v_add_u32_e32 v5, 1, v2
	s_mov_b64 s[14:15], -1
	v_mul_f32_e32 v3, 0x4f7ffffe, v4
	v_cvt_u32_f32_e32 v3, v3
	v_sub_u32_e32 v4, 0, v1
	v_mul_lo_u32 v4, v4, v3
	v_mul_hi_u32 v4, v3, v4
	v_add_u32_e32 v3, v3, v4
	v_mul_hi_u32 v3, v2, v3
	v_mul_lo_u32 v4, v3, v1
	v_sub_u32_e32 v2, v2, v4
	v_add_u32_e32 v6, 1, v3
	v_cmp_ge_u32_e32 vcc, v2, v1
	v_sub_u32_e32 v4, v2, v1
	s_nop 0
	v_cndmask_b32_e32 v3, v3, v6, vcc
	v_cndmask_b32_e32 v2, v2, v4, vcc
	v_add_u32_e32 v4, 1, v3
	v_cmp_ge_u32_e32 vcc, v2, v1
	s_nop 1
	v_cndmask_b32_e32 v4, v3, v4, vcc
	v_mul_lo_u32 v2, v1, v4
	v_add_u32_e32 v1, v2, v1
	v_cmp_ne_u32_e32 vcc, v5, v1
	v_mov_b64_e32 v[2:3], s[12:13]
	s_and_saveexec_b64 s[10:11], vcc
	s_cbranch_execz .LBB0_222
	v_mov_b32_e32 v1, 0
	global_load_dword v2, v1, s[12:13] sc1
	s_mov_b64 s[18:19], 0
	s_waitcnt vmcnt(0)
	v_cmp_eq_u32_e32 vcc, v2, v4
	s_and_saveexec_b64 s[16:17], vcc
	s_cbranch_execz .LBB0_221
	s_add_u32 s14, s8, 0x200
	s_addc_u32 s15, s9, 0
	s_mov_b32 s3, 1
	s_mov_b64 s[8:9], 0
	s_branch .LBB0_214

.LBB0_3030:
	v_readlane_b32 s4, v255, 4
	v_readlane_b32 s5, v255, 5
	s_lshl_b64 s[4:5], s[4:5], 2
	v_readlane_b32 s6, v255, 2
	s_add_u32 s6, s6, s4
	v_readlane_b32 s4, v255, 3
	s_addc_u32 s7, s4, s5
	v_readlane_b32 s4, v255, 6
	s_lshl_b32 s4, s4, 8
	s_add_u32 s4, s6, s4
	s_addc_u32 s5, s7, 0
	v_mov_b32_e32 v1, 0x1000
	v_mov_b32_e32 v3, 1
	global_atomic_add v3, v1, v3, s[4:5] offset:1024 sc0
	v_cvt_f32_u32_e32 v1, v2
	v_sub_u32_e32 v4, 0, v2
	v_rcp_iflag_f32_e32 v1, v1
	s_nop 0
	v_mul_f32_e32 v1, 0x4f7ffffe, v1
	v_cvt_u32_f32_e32 v1, v1
	v_mul_lo_u32 v4, v4, v1
	v_mul_hi_u32 v4, v1, v4
	v_add_u32_e32 v1, v1, v4
	s_waitcnt vmcnt(0)
	v_mul_hi_u32 v1, v3, v1
	v_mul_lo_u32 v4, v1, v2
	v_sub_u32_e32 v4, v3, v4
	v_add_u32_e32 v5, 1, v1
	v_cmp_ge_u32_e32 vcc, v4, v2
	v_add_u32_e32 v3, 1, v3
	s_nop 0
	v_cndmask_b32_e32 v1, v1, v5, vcc
	v_sub_u32_e32 v5, v4, v2
	v_cndmask_b32_e32 v4, v4, v5, vcc
	v_add_u32_e32 v5, 1, v1
	v_cmp_ge_u32_e32 vcc, v4, v2
	s_nop 1
	v_cndmask_b32_e32 v1, v1, v5, vcc
	v_mul_lo_u32 v4, v2, v1
	v_add_u32_e32 v2, v4, v2
	v_cmp_ne_u32_e32 vcc, v3, v2
	s_and_saveexec_b64 s[8:9], vcc
	s_xor_b64 s[8:9], exec, s[8:9]
	s_cbranch_execz .LBB0_3044
	s_waitcnt lgkmcnt(0)
	v_mov_b32_e32 v0, 0x2000
	buffer_inv sc1
	global_load_dword v0, v0, s[4:5] offset:1024 sc1
	s_add_u32 s12, s4, 0x2400
	s_addc_u32 s13, s5, 0
	s_waitcnt vmcnt(0)
	v_cmp_eq_u32_e32 vcc, v0, v1
	s_and_saveexec_b64 s[10:11], vcc
	s_cbranch_execz .LBB0_3043
	s_mov_b32 s28, 1
	s_mov_b64 s[14:15], 0
	v_mov_b32_e32 v0, 0
	s_branch .LBB0_3034

.LBB0_3044:
	s_andn2_saveexec_b64 s[8:9], s[8:9]
	s_cbranch_execz .LBB0_3062
	s_mov_b64 s[8:9], exec
	buffer_wbl2 sc1
	s_waitcnt lgkmcnt(0)
	s_waitcnt vmcnt(0)
	v_mbcnt_lo_u32_b32 v1, s8, 0
	v_mbcnt_hi_u32_b32 v1, s9, v1
	v_cmp_eq_u32_e32 vcc, 0, v1
	s_and_saveexec_b64 s[10:11], vcc
	s_cbranch_execz .LBB0_3047
	s_bcnt1_i32_b64 s8, s[8:9]
	v_mov_b32_e32 v2, 0x3000
	v_mov_b32_e32 v3, s8
	global_atomic_add v2, v2, v3, s[6:7] offset:1024 sc0
	buffer_inv sc1
.LBB0_3047:
	s_or_b64 exec, exec, s[10:11]
	v_cvt_f32_u32_e32 v3, v0
	s_waitcnt vmcnt(1)
	v_readfirstlane_b32 s8, v2
	s_add_u32 s10, s6, 0x3500
	s_addc_u32 s11, s7, 0
	v_rcp_iflag_f32_e32 v3, v3
	v_add_u32_e32 v1, s8, v1
	v_add_u32_e32 v4, 1, v1
	s_mov_b64 s[12:13], -1
	v_mul_f32_e32 v2, 0x4f7ffffe, v3
	v_cvt_u32_f32_e32 v2, v2
	v_sub_u32_e32 v3, 0, v0
	v_mul_lo_u32 v3, v3, v2
	v_mul_hi_u32 v3, v2, v3
	v_add_u32_e32 v2, v2, v3
	v_mul_hi_u32 v2, v1, v2
	v_mul_lo_u32 v3, v2, v0
	v_sub_u32_e32 v1, v1, v3
	v_add_u32_e32 v5, 1, v2
	v_cmp_ge_u32_e32 vcc, v1, v0
	v_sub_u32_e32 v3, v1, v0
	s_nop 0
	v_cndmask_b32_e32 v2, v2, v5, vcc
	v_cndmask_b32_e32 v1, v1, v3, vcc
	v_add_u32_e32 v3, 1, v2
	v_cmp_ge_u32_e32 vcc, v1, v0
	s_nop 1
	v_cndmask_b32_e32 v2, v2, v3, vcc
	v_mul_lo_u32 v1, v0, v2
	v_add_u32_e32 v0, v1, v0
	v_cmp_ne_u32_e32 vcc, v4, v0
	v_mov_b64_e32 v[0:1], s[10:11]
	s_and_saveexec_b64 s[8:9], vcc
	s_cbranch_execz .LBB0_3059
	v_mov_b32_e32 v0, 0
	global_load_dword v1, v0, s[10:11] sc1
	s_mov_b64 s[16:17], 0
	s_waitcnt vmcnt(0)
	v_cmp_eq_u32_e32 vcc, v1, v2
	s_and_saveexec_b64 s[14:15], vcc
	s_cbranch_execz .LBB0_3058
	s_add_u32 s12, s6, 0x200
	s_addc_u32 s13, s7, 0
	s_mov_b32 s28, 1
	s_mov_b64 s[6:7], 0
	s_branch .LBB0_3051
